# MLA step: the step's three tile DMAs are issued after its last P.V MFMA (LDS idle) instead of at the step start
# baseline (speedup 1.0000x reference)
.LBB0_1455:
.LBB0_1456:
	s_add_i32 s2, s79, 1
	s_and_b32 s2, s2, 3
	s_mulk_i32 s2, 0x3000
	v_add_u32_e32 v72, s2, v168
	ds_read_b128 v[68:71], v72
	ds_read_b128 v[172:175], v72 offset:512
	ds_read_b128 v[176:179], v72 offset:2048
	ds_read_b128 v[180:183], v72 offset:2560
	ds_read_b128 v[184:187], v72 offset:4096
	ds_read_b128 v[190:193], v72 offset:4608
	ds_read_b128 v[212:215], v72 offset:6144
	ds_read_b128 v[216:219], v72 offset:6656
	ds_read_b128 v[224:227], v72 offset:8192
	ds_read_b128 v[228:231], v72 offset:8704
	ds_read_b128 v[232:235], v72 offset:10240
	ds_read_b128 v[236:239], v72 offset:10752
	s_waitcnt lgkmcnt(11)
	v_mfma_f32_32x32x16_bf16 v[100:115], v[68:71], v[116:119], v[36:51]
	v_exp_f32_e32 v84, v84
	v_exp_f32_e32 v85, v85
	v_exp_f32_e32 v86, v86
	v_exp_f32_e32 v87, v87
	s_waitcnt lgkmcnt(10)
	v_mfma_f32_32x32x16_bf16 v[68:83], v[172:175], v[116:119], v[36:51]
	v_add_f32_e64 v172, v84, 0
	v_add_f32_e64 v173, v85, 0
	v_add_f32_e64 v172, v86, v172
	v_add_f32_e64 v173, v87, v173
	s_waitcnt lgkmcnt(9)
	v_mfma_f32_32x32x16_bf16 v[100:115], v[176:179], v[120:123], v[100:115]
	v_exp_f32_e32 v88, v88
	v_exp_f32_e32 v89, v89
	v_exp_f32_e32 v90, v90
	v_exp_f32_e32 v91, v91
	v_pk_add_f32 v[172:173], v[88:89], v[172:173]
	s_nop 0
	v_pk_add_f32 v[172:173], v[90:91], v[172:173]
	s_waitcnt lgkmcnt(8)
	v_mfma_f32_32x32x16_bf16 v[68:83], v[180:183], v[120:123], v[68:83]
	s_waitcnt lgkmcnt(7)
	v_mfma_f32_32x32x16_bf16 v[100:115], v[184:187], v[124:127], v[100:115]
	v_exp_f32_e32 v92, v92
	v_exp_f32_e32 v93, v93
	v_exp_f32_e32 v94, v94
	v_exp_f32_e32 v95, v95
	v_pk_add_f32 v[172:173], v[92:93], v[172:173]
	s_nop 0
	v_pk_add_f32 v[172:173], v[94:95], v[172:173]
	s_waitcnt lgkmcnt(6)
	v_mfma_f32_32x32x16_bf16 v[68:83], v[190:193], v[124:127], v[68:83]
	s_waitcnt lgkmcnt(5)
	v_mfma_f32_32x32x16_bf16 v[100:115], v[212:215], v[128:131], v[100:115]
	v_exp_f32_e32 v96, v96
	v_exp_f32_e32 v97, v97
	v_exp_f32_e32 v98, v98
	v_exp_f32_e32 v99, v99
	v_pk_add_f32 v[172:173], v[96:97], v[172:173]
	s_nop 0
	v_pk_add_f32 v[172:173], v[98:99], v[172:173]
	s_waitcnt lgkmcnt(4)
	v_mfma_f32_32x32x16_bf16 v[68:83], v[216:219], v[128:131], v[68:83]
	v_exp_f32_e32 v174, v52
	v_exp_f32_e32 v175, v53
	s_waitcnt lgkmcnt(3)
	v_mfma_f32_32x32x16_bf16 v[100:115], v[224:227], v[132:135], v[100:115]
	v_add_f32_e64 v52, v174, v172
	v_add_f32_e64 v53, v175, v173
	v_exp_f32_e32 v172, v54
	v_exp_f32_e32 v173, v55
	s_nop 0
	v_pk_add_f32 v[52:53], v[172:173], v[52:53]
	s_waitcnt lgkmcnt(2)
	v_mfma_f32_32x32x16_bf16 v[68:83], v[228:231], v[132:135], v[68:83]
	s_waitcnt lgkmcnt(1)
	v_mfma_f32_32x32x16_bf16 v[100:115], v[232:235], v[136:139], v[100:115]
	v_exp_f32_e32 v176, v56
	v_exp_f32_e32 v177, v57
	v_exp_f32_e32 v178, v58
	v_exp_f32_e32 v179, v59
	v_pk_add_f32 v[52:53], v[176:177], v[52:53]
	s_nop 0
	v_pk_add_f32 v[194:195], v[178:179], v[52:53]
	s_waitcnt lgkmcnt(0)
	v_mfma_f32_32x32x16_bf16 v[68:83], v[236:239], v[136:139], v[68:83]
	s_and_b32 s2, s78, 0x4000
	v_add_u32_e32 v212, s2, v2
	v_cvt_pk_bf16_f32 v54, v88, v89
	ds_read_b64_tr_b16 v[88:89],v212 offset:0
	v_cvt_pk_bf16_f32 v55, v90, v91
	ds_read_b64_tr_b16 v[90:91],v212 offset:512
	v_cvt_pk_bf16_f32 v53, v86, v87
	v_cvt_pk_bf16_f32 v86, v176, v177
	ds_read_b64_tr_b16 v[176:177],v212 offset:4096
	v_cvt_pk_bf16_f32 v87, v178, v179
	ds_read_b64_tr_b16 v[178:179],v212 offset:4608
	v_cvt_pk_bf16_f32 v56, v92, v93
	ds_read_b64_tr_b16 v[92:93],v212 offset:1024
	v_cvt_pk_bf16_f32 v57, v94, v95
	ds_read_b64_tr_b16 v[94:95],v212 offset:1536
	ds_read_b64_tr_b16 v[180:181],v212 offset:5120
	ds_read_b64_tr_b16 v[182:183],v212 offset:5632
	v_cvt_pk_bf16_f32 v58, v96, v97
	ds_read_b64_tr_b16 v[96:97],v212 offset:2048
	v_cvt_pk_bf16_f32 v59, v98, v99
	ds_read_b64_tr_b16 v[98:99],v212 offset:2560
	ds_read_b64_tr_b16 v[184:185],v212 offset:6144
	ds_read_b64_tr_b16 v[186:187],v212 offset:6656
	v_cvt_pk_bf16_f32 v52, v84, v85
	v_cvt_pk_bf16_f32 v85, v172, v173
	ds_read_b64_tr_b16 v[172:173],v212 offset:3072
	v_cvt_pk_bf16_f32 v84, v174, v175
	ds_read_b64_tr_b16 v[174:175],v212 offset:3584
	ds_read_b64_tr_b16 v[190:191],v212 offset:7168
	ds_read_b64_tr_b16 v[192:193],v212 offset:7680
	s_waitcnt lgkmcnt(14)
	v_mfma_f32_32x32x16_bf16 v[4:19], v[52:55], v[88:91], v[4:19]
	s_waitcnt lgkmcnt(12)
	v_mfma_f32_32x32x16_bf16 v[20:35], v[52:55], v[176:179], v[20:35]
	v_exp_f32_e32 v52, v60
	v_exp_f32_e32 v53, v61
	v_exp_f32_e32 v60, v62
	v_exp_f32_e32 v61, v63
	v_pk_add_f32 v[54:55], v[52:53], v[194:195]
	s_nop 0
	v_pk_add_f32 v[54:55], v[60:61], v[54:55]
	s_waitcnt lgkmcnt(10)
	v_mfma_f32_32x32x16_bf16 v[4:19], v[56:59], v[92:95], v[4:19]
	v_cvt_pk_bf16_f32 v52, v52, v53
	v_cvt_pk_bf16_f32 v53, v60, v61
	s_waitcnt lgkmcnt(8)
	v_mfma_f32_32x32x16_bf16 v[20:35], v[56:59], v[180:183], v[20:35]
	v_exp_f32_e32 v56, v64
	v_exp_f32_e32 v57, v65
	v_exp_f32_e32 v58, v66
	v_exp_f32_e32 v59, v67
	v_pk_add_f32 v[54:55], v[56:57], v[54:55]
	s_nop 0
	v_pk_add_f32 v[62:63], v[58:59], v[54:55]
	v_cvt_pk_bf16_f32 v54, v56, v57
	v_add_f32_e32 v56, v62, v63
	v_add_f32_e32 v171, v171, v56
	v_cvt_pk_bf16_f32 v55, v58, v59
	s_waitcnt lgkmcnt(6)
	v_mfma_f32_32x32x16_bf16 v[4:19], v[84:87], v[96:99], v[4:19]
	v_max3_f32 v56, v100, v68, v101
	s_nop 0
	v_max3_f32 v56, v56, v69, v102
	s_nop 0
	v_max3_f32 v56, v56, v70, v103
	s_nop 0
	v_max3_f32 v56, v56, v71, v104
	s_waitcnt lgkmcnt(4)
	v_mfma_f32_32x32x16_bf16 v[20:35], v[84:87], v[184:187], v[20:35]
	v_max3_f32 v56, v56, v72, v105
	s_nop 0
	v_max3_f32 v56, v56, v73, v106
	s_nop 0
	v_max3_f32 v56, v56, v74, v107
	s_nop 0
	v_max3_f32 v56, v56, v75, v107
	s_waitcnt lgkmcnt(2)
	v_mfma_f32_32x32x16_bf16 v[4:19], v[52:55], v[172:175], v[4:19]
	s_waitcnt lgkmcnt(0)
	v_mfma_f32_32x32x16_bf16 v[20:35], v[52:55], v[190:193], v[20:35]
	s_cmp_gt_u32 s79, 64
	s_cbranch_scc1 .Lmla_dma_skip1
	s_add_i32 s2, s79, -1
	s_and_b32 s6, s2, 3
	s_mul_i32 s7, s6, 0x3000
	v_lshl_add_u64 v[240:241], v[162:163], 0, s[88:89]
	s_add_i32 s2, s7, s9
	s_mov_b32 s3, m0
	s_mov_b32 m0, s2
	s_nop 0
	global_load_lds_dwordx4 v[240:241], off
	s_mov_b32 m0, s3
	s_movk_i32 s2, 0xf000
	s_mov_b32 s3, -1
	v_lshl_add_u64 v[240:241], v[158:159], 0, s[2:3]
	s_add_i32 s2, s7, s27
	s_mov_b32 s3, m0
	s_mov_b32 m0, s2
	s_nop 0
	global_load_lds_dwordx4 v[240:241], off
	s_mov_b32 m0, s3
	s_lshl_b32 s2, s6, 13
	v_lshl_add_u64 v[240:241], v[160:161], 0, s[88:89]
	s_add_i32 s2, s2, s26
	s_mov_b32 s3, m0
	s_mov_b32 m0, s2
	s_nop 0
	global_load_lds_dwordx4 v[240:241], off
	s_mov_b32 m0, s3
.Lmla_dma_skip1:
	v_max3_f32 v52, v56, v108, v76
	s_nop 0
	v_max3_f32 v52, v52, v109, v77
	s_nop 0
	v_max3_f32 v52, v52, v110, v78
	s_nop 0
	v_max3_f32 v52, v52, v111, v79
	s_nop 0
	v_max3_f32 v52, v52, v112, v80
	s_nop 0
	v_max3_f32 v52, v52, v113, v81
	s_nop 0
	v_max3_f32 v52, v52, v114, v82
	s_nop 0
	v_max3_f32 v52, v52, v115, v83
	s_nop 0
	v_mov_b32_e32 v53, v52
	s_nop 1
	v_permlane32_swap_b32_e32 v52, v53
	v_max_f32_e32 v53, v53, v53
	v_max_f32_e32 v52, v52, v52
	v_max_f32_e32 v52, v52, v53
	v_cmp_lt_f32_e32 vcc, s13, v52
	s_cbranch_vccz .LBB0_1460
	v_max_f32_e32 v52, v52, v52
	v_max_f32_e32 v52, 0, v52
	v_exp_f32_e64 v53, -v52
	s_and_saveexec_b64 s[6:7], s[36:37]
	ds_write_b32 v170, v53
	s_or_b64 exec, exec, s[6:7]
	v_mul_f32_e32 v171, v171, v53
	s_waitcnt lgkmcnt(0)
	v_add_u32_e32 v53, s28, v169
	ds_read_b128 v[54:57], v53
	ds_read_b128 v[58:61], v53 offset:32
	ds_read_b128 v[62:65], v53 offset:64
	ds_read_b128 v[84:87], v53 offset:96
	s_waitcnt lgkmcnt(0)
	s_waitcnt lgkmcnt(3)
	v_pk_mul_f32 v[6:7], v[6:7], v[56:57]
	s_waitcnt lgkmcnt(2)
	v_pk_mul_f32 v[8:9], v[8:9], v[58:59]
	s_waitcnt lgkmcnt(1)
	v_pk_mul_f32 v[12:13], v[12:13], v[62:63]
	s_waitcnt lgkmcnt(0)
	v_pk_mul_f32 v[16:17], v[16:17], v[84:85]
	v_pk_mul_f32 v[18:19], v[18:19], v[86:87]
	v_pk_mul_f32 v[14:15], v[14:15], v[64:65]
	v_pk_mul_f32 v[10:11], v[10:11], v[60:61]
	v_pk_mul_f32 v[4:5], v[4:5], v[54:55]
	v_pk_mul_f32 v[32:33], v[32:33], v[84:85]
	v_pk_mul_f32 v[28:29], v[28:29], v[62:63]
	v_pk_mul_f32 v[24:25], v[24:25], v[58:59]
	v_pk_mul_f32 v[34:35], v[34:35], v[86:87]
	v_pk_mul_f32 v[30:31], v[30:31], v[64:65]
	v_pk_mul_f32 v[26:27], v[26:27], v[60:61]
	v_pk_mul_f32 v[22:23], v[22:23], v[56:57]
	v_pk_mul_f32 v[20:21], v[20:21], v[54:55]
	v_sub_f32_e32 v115, v115, v52
	v_sub_f32_e32 v114, v114, v52
	v_sub_f32_e32 v113, v113, v52
	v_sub_f32_e32 v112, v112, v52
	v_sub_f32_e32 v111, v111, v52
	v_sub_f32_e32 v110, v110, v52
	v_sub_f32_e32 v109, v109, v52
	v_sub_f32_e32 v108, v108, v52
	v_sub_f32_e32 v107, v107, v52
	v_sub_f32_e32 v106, v106, v52
	v_sub_f32_e32 v105, v105, v52
	v_sub_f32_e32 v104, v104, v52
	v_sub_f32_e32 v103, v103, v52
	v_sub_f32_e32 v102, v102, v52
	v_sub_f32_e32 v101, v101, v52
	v_sub_f32_e32 v100, v100, v52
	v_sub_f32_e32 v83, v83, v52
	v_sub_f32_e32 v82, v82, v52
	v_sub_f32_e32 v81, v81, v52
	v_sub_f32_e32 v80, v80, v52
	v_sub_f32_e32 v79, v79, v52
	v_sub_f32_e32 v78, v78, v52
	v_sub_f32_e32 v77, v77, v52
	v_sub_f32_e32 v76, v76, v52
	v_sub_f32_e32 v75, v75, v52
	v_sub_f32_e32 v74, v74, v52
	v_sub_f32_e32 v73, v73, v52
	v_sub_f32_e32 v72, v72, v52
	v_sub_f32_e32 v71, v71, v52
	v_sub_f32_e32 v70, v70, v52
	v_sub_f32_e32 v69, v69, v52
	v_sub_f32_e32 v68, v68, v52
	v_sub_f32_e32 v51, v51, v52
	v_sub_f32_e32 v50, v50, v52
	v_sub_f32_e32 v49, v49, v52
	v_sub_f32_e32 v48, v48, v52
	v_sub_f32_e32 v47, v47, v52
	v_sub_f32_e32 v46, v46, v52
	v_sub_f32_e32 v45, v45, v52
	v_sub_f32_e32 v44, v44, v52
	v_sub_f32_e32 v43, v43, v52
	v_sub_f32_e32 v42, v42, v52
	v_sub_f32_e32 v41, v41, v52
	v_sub_f32_e32 v40, v40, v52
	v_sub_f32_e32 v39, v39, v52
	v_sub_f32_e32 v38, v38, v52
	v_sub_f32_e32 v37, v37, v52
	v_sub_f32_e32 v36, v36, v52

.LBB0_1463:
.LBB0_1464:
	s_add_i32 s79, s79, 2
	s_and_b32 s2, s79, 2
	s_mulk_i32 s2, 0x3000
	v_add_u32_e32 v56, s2, v168
	ds_read_b128 v[52:55], v56
	ds_read_b128 v[172:175], v56 offset:512
	ds_read_b128 v[176:179], v56 offset:2048
	ds_read_b128 v[180:183], v56 offset:2560
	ds_read_b128 v[184:187], v56 offset:4096
	ds_read_b128 v[190:193], v56 offset:4608
	ds_read_b128 v[212:215], v56 offset:6144
	ds_read_b128 v[216:219], v56 offset:6656
	ds_read_b128 v[224:227], v56 offset:8192
	ds_read_b128 v[228:231], v56 offset:8704
	ds_read_b128 v[232:235], v56 offset:10240
	ds_read_b128 v[236:239], v56 offset:10752
	s_waitcnt lgkmcnt(11)
	v_mfma_f32_32x32x16_bf16 v[84:99], v[52:55], v[116:119], v[36:51]
	v_exp_f32_e32 v100, v100
	v_exp_f32_e32 v101, v101
	v_exp_f32_e32 v102, v102
	v_exp_f32_e32 v103, v103
	s_waitcnt lgkmcnt(10)
	v_mfma_f32_32x32x16_bf16 v[52:67], v[172:175], v[116:119], v[36:51]
	v_add_f32_e64 v172, v100, 0
	v_add_f32_e64 v173, v101, 0
	v_add_f32_e64 v172, v102, v172
	v_add_f32_e64 v173, v103, v173
	s_waitcnt lgkmcnt(9)
	v_mfma_f32_32x32x16_bf16 v[84:99], v[176:179], v[120:123], v[84:99]
	v_exp_f32_e32 v104, v104
	v_exp_f32_e32 v105, v105
	v_exp_f32_e32 v106, v106
	v_exp_f32_e32 v107, v107
	v_pk_add_f32 v[172:173], v[104:105], v[172:173]
	s_nop 0
	v_pk_add_f32 v[172:173], v[106:107], v[172:173]
	s_waitcnt lgkmcnt(8)
	v_mfma_f32_32x32x16_bf16 v[52:67], v[180:183], v[120:123], v[52:67]
	s_waitcnt lgkmcnt(7)
	v_mfma_f32_32x32x16_bf16 v[84:99], v[184:187], v[124:127], v[84:99]
	v_exp_f32_e32 v108, v108
	v_exp_f32_e32 v109, v109
	v_exp_f32_e32 v110, v110
	v_exp_f32_e32 v111, v111
	v_pk_add_f32 v[172:173], v[108:109], v[172:173]
	s_nop 0
	v_pk_add_f32 v[172:173], v[110:111], v[172:173]
	s_waitcnt lgkmcnt(6)
	v_mfma_f32_32x32x16_bf16 v[52:67], v[190:193], v[124:127], v[52:67]
	s_waitcnt lgkmcnt(5)
	v_mfma_f32_32x32x16_bf16 v[84:99], v[212:215], v[128:131], v[84:99]
	v_exp_f32_e32 v112, v112
	v_exp_f32_e32 v113, v113
	v_exp_f32_e32 v114, v114
	v_exp_f32_e32 v115, v115
	v_pk_add_f32 v[172:173], v[112:113], v[172:173]
	s_nop 0
	v_pk_add_f32 v[172:173], v[114:115], v[172:173]
	s_waitcnt lgkmcnt(4)
	v_mfma_f32_32x32x16_bf16 v[52:67], v[216:219], v[128:131], v[52:67]
	v_exp_f32_e32 v174, v68
	v_exp_f32_e32 v175, v69
	s_waitcnt lgkmcnt(3)
	v_mfma_f32_32x32x16_bf16 v[84:99], v[224:227], v[132:135], v[84:99]
	v_add_f32_e64 v68, v174, v172
	v_add_f32_e64 v69, v175, v173
	v_exp_f32_e32 v172, v70
	v_exp_f32_e32 v173, v71
	s_nop 0
	v_pk_add_f32 v[68:69], v[172:173], v[68:69]
	s_waitcnt lgkmcnt(2)
	v_mfma_f32_32x32x16_bf16 v[52:67], v[228:231], v[132:135], v[52:67]
	s_waitcnt lgkmcnt(1)
	v_mfma_f32_32x32x16_bf16 v[84:99], v[232:235], v[136:139], v[84:99]
	v_exp_f32_e32 v176, v72
	v_exp_f32_e32 v177, v73
	v_exp_f32_e32 v178, v74
	v_exp_f32_e32 v179, v75
	v_pk_add_f32 v[68:69], v[176:177], v[68:69]
	s_nop 0
	v_pk_add_f32 v[194:195], v[178:179], v[68:69]
	s_waitcnt lgkmcnt(0)
	v_mfma_f32_32x32x16_bf16 v[52:67], v[236:239], v[136:139], v[52:67]
	s_add_i32 s2, s78, 0x2000
	s_and_b32 s2, s2, 0x6000
	v_add_u32_e32 v212, s2, v2
	v_cvt_pk_bf16_f32 v70, v104, v105
	ds_read_b64_tr_b16 v[104:105],v212 offset:0
	v_cvt_pk_bf16_f32 v71, v106, v107
	ds_read_b64_tr_b16 v[106:107],v212 offset:512
	v_cvt_pk_bf16_f32 v69, v102, v103
	v_cvt_pk_bf16_f32 v102, v176, v177
	ds_read_b64_tr_b16 v[176:177],v212 offset:4096
	v_cvt_pk_bf16_f32 v103, v178, v179
	ds_read_b64_tr_b16 v[178:179],v212 offset:4608
	v_cvt_pk_bf16_f32 v72, v108, v109
	ds_read_b64_tr_b16 v[108:109],v212 offset:1024
	v_cvt_pk_bf16_f32 v73, v110, v111
	ds_read_b64_tr_b16 v[110:111],v212 offset:1536
	ds_read_b64_tr_b16 v[180:181],v212 offset:5120
	ds_read_b64_tr_b16 v[182:183],v212 offset:5632
	v_cvt_pk_bf16_f32 v74, v112, v113
	ds_read_b64_tr_b16 v[112:113],v212 offset:2048
	v_cvt_pk_bf16_f32 v75, v114, v115
	ds_read_b64_tr_b16 v[114:115],v212 offset:2560
	ds_read_b64_tr_b16 v[184:185],v212 offset:6144
	ds_read_b64_tr_b16 v[186:187],v212 offset:6656
	v_cvt_pk_bf16_f32 v68, v100, v101
	v_cvt_pk_bf16_f32 v101, v172, v173
	ds_read_b64_tr_b16 v[172:173],v212 offset:3072
	v_cvt_pk_bf16_f32 v100, v174, v175
	ds_read_b64_tr_b16 v[174:175],v212 offset:3584
	ds_read_b64_tr_b16 v[190:191],v212 offset:7168
	ds_read_b64_tr_b16 v[192:193],v212 offset:7680
	s_waitcnt lgkmcnt(14)
	v_mfma_f32_32x32x16_bf16 v[4:19], v[68:71], v[104:107], v[4:19]
	s_waitcnt lgkmcnt(12)
	v_mfma_f32_32x32x16_bf16 v[20:35], v[68:71], v[176:179], v[20:35]
	v_exp_f32_e32 v68, v76
	v_exp_f32_e32 v69, v77
	v_exp_f32_e32 v76, v78
	v_exp_f32_e32 v77, v79
	v_pk_add_f32 v[70:71], v[68:69], v[194:195]
	s_nop 0
	v_pk_add_f32 v[70:71], v[76:77], v[70:71]
	s_waitcnt lgkmcnt(10)
	v_mfma_f32_32x32x16_bf16 v[4:19], v[72:75], v[108:111], v[4:19]
	v_cvt_pk_bf16_f32 v68, v68, v69
	v_cvt_pk_bf16_f32 v69, v76, v77
	s_waitcnt lgkmcnt(8)
	v_mfma_f32_32x32x16_bf16 v[20:35], v[72:75], v[180:183], v[20:35]
	v_exp_f32_e32 v72, v80
	v_exp_f32_e32 v73, v81
	v_exp_f32_e32 v74, v82
	v_exp_f32_e32 v75, v83
	v_pk_add_f32 v[70:71], v[72:73], v[70:71]
	s_nop 0
	v_pk_add_f32 v[78:79], v[74:75], v[70:71]
	v_cvt_pk_bf16_f32 v70, v72, v73
	v_add_f32_e32 v72, v78, v79
	v_add_f32_e32 v171, v171, v72
	v_cvt_pk_bf16_f32 v71, v74, v75
	s_waitcnt lgkmcnt(6)
	v_mfma_f32_32x32x16_bf16 v[4:19], v[100:103], v[112:115], v[4:19]
	v_max3_f32 v72, v84, v52, v85
	s_nop 0
	v_max3_f32 v72, v72, v53, v86
	s_nop 0
	v_max3_f32 v72, v72, v54, v87
	s_nop 0
	v_max3_f32 v72, v72, v55, v88
	s_waitcnt lgkmcnt(4)
	v_mfma_f32_32x32x16_bf16 v[20:35], v[100:103], v[184:187], v[20:35]
	v_max3_f32 v72, v72, v56, v89
	s_nop 0
	v_max3_f32 v72, v72, v57, v90
	s_nop 0
	v_max3_f32 v72, v72, v58, v91
	s_nop 0
	v_max3_f32 v72, v72, v59, v91
	s_waitcnt lgkmcnt(2)
	v_mfma_f32_32x32x16_bf16 v[4:19], v[68:71], v[172:175], v[4:19]
	s_waitcnt lgkmcnt(0)
	v_mfma_f32_32x32x16_bf16 v[20:35], v[68:71], v[190:193], v[20:35]
	s_cmp_gt_u32 s79, 65
	s_cbranch_scc1 .Lmla_dma_skip2
	s_and_b32 s2, s79, 2
	s_xor_b32 s2, s2, 2
	s_mul_i32 s3, s2, 0x3000
	s_add_i32 s6, s3, s9
	s_mov_b32 s7, m0
	s_mov_b32 m0, s6
	s_nop 0
	global_load_lds_dwordx4 v[162:163], off
	s_mov_b32 m0, s7
	s_add_i32 s3, s3, s27
	s_mov_b32 s6, m0
	s_mov_b32 m0, s3
	s_nop 0
	global_load_lds_dwordx4 v[158:159], off
	s_mov_b32 m0, s6
	s_lshl_b32 s2, s2, 13
	s_add_i32 s2, s2, s26
	s_mov_b32 s3, m0
	s_mov_b32 m0, s2
	s_nop 0
	global_load_lds_dwordx4 v[160:161], off
	s_mov_b32 m0, s3
.Lmla_dma_skip2:
	v_max3_f32 v68, v72, v92, v60
	s_nop 0
	v_max3_f32 v68, v68, v93, v61
	s_nop 0
	v_max3_f32 v68, v68, v94, v62
	s_nop 0
	v_max3_f32 v68, v68, v95, v63
	s_nop 0
	v_max3_f32 v68, v68, v96, v64
	s_nop 0
	v_max3_f32 v68, v68, v97, v65
	s_nop 0
	v_max3_f32 v68, v68, v98, v66
	s_nop 0
	v_max3_f32 v68, v68, v99, v67
	s_nop 0
	v_mov_b32_e32 v69, v68
	s_nop 1
	v_permlane32_swap_b32_e32 v68, v69
	s_andn2_b64 vcc, exec, s[62:63]
	s_cbranch_vccnz .LBB0_1451
	v_max_f32_e32 v68, v68, v68
	v_max_f32_e32 v69, v69, v69
	v_max_f32_e32 v68, v68, v69
	v_cmp_lt_f32_e32 vcc, s13, v68
	s_cbranch_vccz .LBB0_1451
	v_max_f32_e32 v68, v68, v68
	v_max_f32_e32 v68, 0, v68
	v_exp_f32_e64 v69, -v68
	s_and_saveexec_b64 s[6:7], s[36:37]
	s_cbranch_execz .LBB0_1450
	ds_write_b32 v170, v69
	s_branch .LBB0_1450
